# attention chunk epilogue: row halves exchanged with v_permlane32_swap, 4 global_store_dwordx4 per lane instead of 8 dwordx2
# baseline (speedup 1.0000x reference)
; DI unsigned pk2(float lo, float hi) { f32x2 v = {lo, hi}; return __builtin_bit_cast(unsigned, __builtin_convertvector(v, bf16v2)); }
;     ...
;             float lsum = (ls0 + ls1) + (ls2 + ls3);
; #pragma unroll
;             for (int kk = 0; kk < 4; ++kk) asm volatile("" : "+v"(qfn[kk]));
;             asm volatile("" : "+v"(enn));
;             const float mx = mrun;
;             lsum += __shfl_xor(lsum, 32);
;             const float inv = 1.0f / lsum;
;             if (valid) {
;                 int hf = half; asm volatile("" : "+v"(hf));
;                 bf16_t* op = PO + ((size_t)slot * T + tok) * CW + h * 64 + 4 * hf;
; #pragma unroll
;                 for (int dt = 0; dt < 2; ++dt)
; #pragma unroll
;                     for (int ig = 0; ig < 4; ++ig) { u32x2 w; w.x = pk2(oacc[dt][4 * ig] * inv, oacc[dt][4 * ig + 1] * inv); w.y = pk2(oacc[dt][4 * ig + 2] * inv, oacc[dt][4 * ig + 3] * inv);
;                         *(u32x2*)(op + 32 * dt + 8 * ig) = w; }
;                 if (half == 0) PST[((size_t)slot * T + tok) * 8 + h] = (f32x2){mx, lsum};
;             }
.LBB0_2238:
	v_lshl_or_b32 v33, s20, 5, v149
	v_cmp_lt_i32_e32 vcc, v33, v245
	v_add_f32_e32 v33, v120, v121
	s_waitcnt lgkmcnt(0)
	v_add_f32_e32 v34, v118, v119
	v_add_f32_e32 v33, v34, v33
	s_nop 0
	v_mov_b32_e32 v34, v33
	s_nop 1
	v_permlane32_swap_b32_e32 v34, v33
	s_waitcnt vmcnt(3)
	s_waitcnt vmcnt(2)
	s_waitcnt vmcnt(1)
	s_waitcnt vmcnt(0)
	s_and_saveexec_b64 s[6:7], vcc
	s_cbranch_execz .LBB0_2225
	s_waitcnt lgkmcnt(0)
	v_add_f32_e32 v33, v33, v34
	v_div_scale_f32 v34, s[20:21], v33, v33, 1.0
	v_rcp_f32_e32 v35, v34
	v_div_scale_f32 v36, vcc, 1.0, v33, 1.0
	v_fma_f32 v37, -v34, v35, 1.0
	v_fmac_f32_e32 v35, v37, v35
	v_mul_f32_e32 v37, v36, v35
	v_fma_f32 v38, -v34, v37, v36
	v_fmac_f32_e32 v37, v38, v35
	v_fma_f32 v34, -v34, v37, v36
	v_mov_b32_e32 v36, 15
	v_lshlrev_b32_sdwa v36, v36, v248 dst_sel:DWORD dst_unused:UNUSED_PAD src0_sel:DWORD src1_sel:WORD_1
	v_div_fmas_f32 v34, v34, v35, v37
	v_mov_b32_e32 v35, v151
	v_add3_u32 v64, v249, s44, v36
	v_div_fixup_f32 v34, v34, v33, 1.0
	v_lshlrev_b64 v[36:37], 10, v[64:65]
	v_lshlrev_b32_e32 v38, 3, v35
	v_lshl_add_u64 v[36:37], s[0:1], 0, v[36:37]
	v_ashrrev_i32_e32 v39, 31, v38
	v_mul_f32_e32 v16, v34, v16
	v_mul_f32_e32 v17, v34, v17
	v_mul_f32_e32 v18, v34, v18
	v_mul_f32_e32 v19, v34, v19
	v_cvt_pk_bf16_f32 v16, v16, v17
	v_cvt_pk_bf16_f32 v17, v18, v19
	v_mul_f32_e32 v20, v34, v20
	v_mul_f32_e32 v21, v34, v21
	v_mul_f32_e32 v22, v34, v22
	v_mul_f32_e32 v23, v34, v23
	v_cvt_pk_bf16_f32 v18, v20, v21
	v_cvt_pk_bf16_f32 v19, v22, v23
	v_mul_f32_e32 v0, v34, v0
	v_mul_f32_e32 v1, v34, v1
	v_mul_f32_e32 v2, v34, v2
	v_mul_f32_e32 v3, v34, v3
	v_cvt_pk_bf16_f32 v0, v0, v1
	v_cvt_pk_bf16_f32 v1, v2, v3
	v_mul_f32_e32 v4, v34, v4
	v_mul_f32_e32 v5, v34, v5
	v_mul_f32_e32 v6, v34, v6
	v_mul_f32_e32 v7, v34, v7
	v_cvt_pk_bf16_f32 v2, v4, v5
	v_cvt_pk_bf16_f32 v3, v6, v7
	v_lshl_add_u64 v[36:37], v[38:39], 1, v[36:37]
	v_mul_f32_e32 v24, v34, v24
	v_mul_f32_e32 v25, v34, v25
	v_mul_f32_e32 v26, v34, v26
	v_mul_f32_e32 v27, v34, v27
	v_cvt_pk_bf16_f32 v24, v24, v25
	v_cvt_pk_bf16_f32 v25, v26, v27
	v_mul_f32_e32 v28, v34, v28
	v_mul_f32_e32 v29, v34, v29
	v_mul_f32_e32 v30, v34, v30
	v_mul_f32_e32 v31, v34, v31
	v_cvt_pk_bf16_f32 v26, v28, v29
	v_cvt_pk_bf16_f32 v27, v30, v31
	v_mul_f32_e32 v8, v34, v8
	v_mul_f32_e32 v9, v34, v9
	v_mul_f32_e32 v10, v34, v10
	v_mul_f32_e32 v11, v34, v11
	v_cvt_pk_bf16_f32 v8, v8, v9
	v_cvt_pk_bf16_f32 v9, v10, v11
	v_mul_f32_e32 v12, v34, v12
	v_mul_f32_e32 v13, v34, v13
	v_mul_f32_e32 v14, v34, v14
	v_mul_f32_e32 v15, v34, v15
	v_cvt_pk_bf16_f32 v10, v12, v13
	v_cvt_pk_bf16_f32 v11, v14, v15
	s_nop 1
	v_permlane32_swap_b32_e32 v16, v18
	v_permlane32_swap_b32_e32 v17, v19
	v_permlane32_swap_b32_e32 v0, v2
	v_permlane32_swap_b32_e32 v1, v3
	v_permlane32_swap_b32_e32 v24, v26
	v_permlane32_swap_b32_e32 v25, v27
	v_permlane32_swap_b32_e32 v8, v10
	v_permlane32_swap_b32_e32 v9, v11
	global_store_dwordx4 v[36:37], v[16:19], off
	global_store_dwordx4 v[36:37], v[0:3], off offset:64
	global_store_dwordx4 v[36:37], v[24:27], off offset:32
	global_store_dwordx4 v[36:37], v[8:11], off offset:96
	s_and_b64 exec, exec, s[12:13]
	s_cbranch_execz .LBB0_2225
	v_lshlrev_b64 v[0:1], 6, v[64:65]
	v_lshl_add_u64 v[0:1], s[2:3], 0, v[0:1]
	global_store_dwordx2 v[0:1], v[32:33], off
	s_branch .LBB0_2225
